# speedup vs baseline: 1.0070x; 1.0070x over previous
.Lred_skip_0:
	s_nop 5
	v_med3_f32 v120, v120, s55, v232
	v_med3_f32 v121, v121, s55, v232
	v_mfma_f32_16x16x32_bf16 v[130:133], v[102:105], v[134:137], v[130:133]
	v_exp_f32_e32 v126, v126
	v_exp_f32_e32 v127, v127
	v_mfma_f32_16x16x32_bf16 v[130:133], v[106:109], v[138:141], v[130:133]
	v_exp_f32_e32 v116, v116
	v_exp_f32_e32 v117, v117
	v_exp_f32_e32 v120, v120
	v_exp_f32_e32 v121, v121
	v_med3_f32 v122, v122, s55, v232
	v_med3_f32 v123, v123, s55, v232
	v_pk_add_f32 v[126:127], v[126:127], 1.0 op_sel_hi:[1,0]
	v_pk_add_f32 v[134:135], v[120:121], 1.0 op_sel_hi:[1,0]
	v_pk_add_f32 v[116:117], v[116:117], 1.0 op_sel_hi:[1,0]
	v_pk_add_f32 v[120:121], v[120:121], 1.0 op_sel_hi:[1,0] neg_lo:[1,0] neg_hi:[1,0]
	v_exp_f32_e32 v128, v128
	v_exp_f32_e32 v129, v129
	v_exp_f32_e32 v118, v118
	v_exp_f32_e32 v119, v119
	v_exp_f32_e32 v122, v122
	v_exp_f32_e32 v123, v123
	v_pk_mul_f32 v[126:127], v[126:127], v[134:135]
	v_exp_f32_e32 v130, v130
	v_exp_f32_e32 v131, v131
	v_pk_add_f32 v[128:129], v[128:129], 1.0 op_sel_hi:[1,0]
	v_pk_add_f32 v[136:137], v[122:123], 1.0 op_sel_hi:[1,0]
	v_pk_add_f32 v[118:119], v[118:119], 1.0 op_sel_hi:[1,0]
	v_pk_add_f32 v[122:123], v[122:123], 1.0 op_sel_hi:[1,0] neg_lo:[1,0] neg_hi:[1,0]
	v_rcp_f32_e32 v126, v126
	v_rcp_f32_e32 v127, v127
	v_rcp_f32_e32 v116, v116
	v_rcp_f32_e32 v117, v117
	v_pk_mul_f32 v[128:129], v[128:129], v[136:137]
	v_exp_f32_e32 v132, v132
	v_exp_f32_e32 v133, v133
	v_pk_mul_f32 v[120:121], v[120:121], v[126:127]
	v_pk_add_f32 v[130:131], v[130:131], 1.0 op_sel_hi:[1,0]
	v_rcp_f32_e32 v128, v128
	v_rcp_f32_e32 v129, v129
	v_rcp_f32_e32 v118, v118
	v_rcp_f32_e32 v119, v119
	v_pk_fma_f32 v[168:169], v[168:169], v[116:117], v[120:121]
	v_pk_mul_f32 v[122:123], v[122:123], v[128:129]
	v_pk_add_f32 v[132:133], v[132:133], 1.0 op_sel_hi:[1,0]
	v_pk_mul_f32 v[134:135], v[168:169], s[78:79]
	v_pk_fma_f32 v[170:171], v[170:171], v[118:119], v[122:123]
	v_med3_f32 v134, v134, s55, v232
	v_med3_f32 v135, v135, s55, v232
	v_pk_mul_f32 v[136:137], v[170:171], s[78:79]
	v_lshl_add_u64 v[122:123], v[166:167], 1, s[30:31]
	v_exp_f32_e32 v134, v134
	v_exp_f32_e32 v135, v135
	v_med3_f32 v136, v136, s55, v232
	v_med3_f32 v137, v137, s55, v232
	v_pk_add_f32 v[126:127], v[134:135], 1.0 op_sel_hi:[1,0]
	v_pk_add_f32 v[134:135], v[134:135], 1.0 op_sel_hi:[1,0] neg_lo:[1,0] neg_hi:[1,0]
	v_exp_f32_e32 v136, v136
	v_exp_f32_e32 v137, v137
	v_pk_mul_f32 v[130:131], v[130:131], v[126:127]
	v_pk_add_f32 v[128:129], v[136:137], 1.0 op_sel_hi:[1,0]
	v_pk_add_f32 v[136:137], v[136:137], 1.0 op_sel_hi:[1,0] neg_lo:[1,0] neg_hi:[1,0]
	v_rcp_f32_e32 v130, v130
	v_rcp_f32_e32 v131, v131
	v_pk_mul_f32 v[132:133], v[132:133], v[128:129]
	v_pk_mul_f32 v[134:135], v[134:135], v[130:131]
	v_rcp_f32_e32 v132, v132
	v_rcp_f32_e32 v133, v133
	v_cvt_pk_bf16_f32 v120, v134, v135
	v_pk_mul_f32 v[136:137], v[136:137], v[132:133]
	v_pk_mul_f32 v[134:135], v[162:163], v[134:135]
	v_cvt_pk_bf16_f32 v121, v136, v137
	v_cvt_pk_bf16_f32 v116, v134, v135
	v_pk_mul_f32 v[136:137], v[164:165], v[136:137]
	global_store_dwordx2 v[122:123], v[120:121], off nt
	v_cvt_pk_bf16_f32 v117, v136, v137
	ds_write_b64 v205, v[116:117] offset:4608
	s_and_b64 s[72:73], exec, s[6:7]
	s_cbranch_scc1 .Lpf_skip_1
	ds_read_b128 v[250:253], v199 offset:9216
	ds_read_b128 v[120:123], v198 offset:57600
	ds_read_b128 v[124:127], v199 offset:9344
	ds_read_b128 v[246:249], v199 offset:9280
	ds_read_b128 v[128:131], v199 offset:9408

.Lred_skip_1:
	s_nop 5
	v_med3_f32 v120, v120, s55, v232
	v_med3_f32 v121, v121, s55, v232
	v_mfma_f32_16x16x32_bf16 v[130:133], v[102:105], v[134:137], v[130:133]
	v_exp_f32_e32 v126, v126
	v_exp_f32_e32 v127, v127
	v_mfma_f32_16x16x32_bf16 v[130:133], v[106:109], v[138:141], v[130:133]
	v_exp_f32_e32 v116, v116
	v_exp_f32_e32 v117, v117
	v_exp_f32_e32 v120, v120
	v_exp_f32_e32 v121, v121
	v_med3_f32 v122, v122, s55, v232
	v_med3_f32 v123, v123, s55, v232
	v_pk_add_f32 v[126:127], v[126:127], 1.0 op_sel_hi:[1,0]
	v_pk_add_f32 v[134:135], v[120:121], 1.0 op_sel_hi:[1,0]
	v_pk_add_f32 v[116:117], v[116:117], 1.0 op_sel_hi:[1,0]
	v_pk_add_f32 v[120:121], v[120:121], 1.0 op_sel_hi:[1,0] neg_lo:[1,0] neg_hi:[1,0]
	v_exp_f32_e32 v128, v128
	v_exp_f32_e32 v129, v129
	v_exp_f32_e32 v118, v118
	v_exp_f32_e32 v119, v119
	v_exp_f32_e32 v122, v122
	v_exp_f32_e32 v123, v123
	v_pk_mul_f32 v[126:127], v[126:127], v[134:135]
	v_exp_f32_e32 v130, v130
	v_exp_f32_e32 v131, v131
	v_pk_add_f32 v[128:129], v[128:129], 1.0 op_sel_hi:[1,0]
	v_pk_add_f32 v[136:137], v[122:123], 1.0 op_sel_hi:[1,0]
	v_pk_add_f32 v[118:119], v[118:119], 1.0 op_sel_hi:[1,0]
	v_pk_add_f32 v[122:123], v[122:123], 1.0 op_sel_hi:[1,0] neg_lo:[1,0] neg_hi:[1,0]
	v_rcp_f32_e32 v126, v126
	v_rcp_f32_e32 v127, v127
	v_rcp_f32_e32 v116, v116
	v_rcp_f32_e32 v117, v117
	v_pk_mul_f32 v[128:129], v[128:129], v[136:137]
	v_exp_f32_e32 v132, v132
	v_exp_f32_e32 v133, v133
	v_pk_mul_f32 v[120:121], v[120:121], v[126:127]
	v_pk_add_f32 v[130:131], v[130:131], 1.0 op_sel_hi:[1,0]
	v_rcp_f32_e32 v128, v128
	v_rcp_f32_e32 v129, v129
	v_rcp_f32_e32 v118, v118
	v_rcp_f32_e32 v119, v119
	v_pk_fma_f32 v[168:169], v[168:169], v[116:117], v[120:121]
	v_pk_mul_f32 v[122:123], v[122:123], v[128:129]
	v_pk_add_f32 v[132:133], v[132:133], 1.0 op_sel_hi:[1,0]
	v_pk_mul_f32 v[134:135], v[168:169], s[78:79]
	v_pk_fma_f32 v[170:171], v[170:171], v[118:119], v[122:123]
	v_med3_f32 v134, v134, s55, v232
	v_med3_f32 v135, v135, s55, v232
	v_pk_mul_f32 v[136:137], v[170:171], s[78:79]
	v_add_u32_e32 v122, 0x80, v166
	v_mov_b32_e32 v123, v114
	v_lshl_add_u64 v[122:123], v[122:123], 1, s[30:31]
	v_exp_f32_e32 v134, v134
	v_exp_f32_e32 v135, v135
	v_med3_f32 v136, v136, s55, v232
	v_med3_f32 v137, v137, s55, v232
	v_pk_add_f32 v[126:127], v[134:135], 1.0 op_sel_hi:[1,0]
	v_pk_add_f32 v[134:135], v[134:135], 1.0 op_sel_hi:[1,0] neg_lo:[1,0] neg_hi:[1,0]
	v_exp_f32_e32 v136, v136
	v_exp_f32_e32 v137, v137
	v_pk_mul_f32 v[130:131], v[130:131], v[126:127]
	v_pk_add_f32 v[128:129], v[136:137], 1.0 op_sel_hi:[1,0]
	v_pk_add_f32 v[136:137], v[136:137], 1.0 op_sel_hi:[1,0] neg_lo:[1,0] neg_hi:[1,0]
	v_rcp_f32_e32 v130, v130
	v_rcp_f32_e32 v131, v131
	v_pk_mul_f32 v[132:133], v[132:133], v[128:129]
	v_pk_mul_f32 v[134:135], v[134:135], v[130:131]
	v_rcp_f32_e32 v132, v132
	v_rcp_f32_e32 v133, v133
	v_cvt_pk_bf16_f32 v120, v134, v135
	v_pk_mul_f32 v[136:137], v[136:137], v[132:133]
	v_pk_mul_f32 v[134:135], v[162:163], v[134:135]
	v_cvt_pk_bf16_f32 v121, v136, v137
	v_cvt_pk_bf16_f32 v116, v134, v135
	v_pk_mul_f32 v[136:137], v[164:165], v[136:137]
	global_store_dwordx2 v[122:123], v[120:121], off nt
	v_cvt_pk_bf16_f32 v117, v136, v137
	ds_write_b64 v205, v[116:117]
	s_and_b64 s[72:73], exec, s[6:7]
	s_cbranch_scc1 .Lpf_skip_2
	ds_read_b128 v[250:253], v199 offset:9216
	ds_read_b128 v[120:123], v198 offset:57600
	ds_read_b128 v[124:127], v199 offset:9344
	ds_read_b128 v[246:249], v199 offset:9280
	ds_read_b128 v[128:131], v199 offset:9408

.Lred_skip_2:
	s_nop 5
	v_med3_f32 v120, v120, s55, v232
	v_med3_f32 v121, v121, s55, v232
	v_mfma_f32_16x16x32_bf16 v[130:133], v[102:105], v[134:137], v[130:133]
	v_exp_f32_e32 v126, v126
	v_exp_f32_e32 v127, v127
	v_mfma_f32_16x16x32_bf16 v[130:133], v[106:109], v[138:141], v[130:133]
	v_exp_f32_e32 v116, v116
	v_exp_f32_e32 v117, v117
	v_exp_f32_e32 v120, v120
	v_exp_f32_e32 v121, v121
	v_med3_f32 v122, v122, s55, v232
	v_med3_f32 v123, v123, s55, v232
	v_pk_add_f32 v[126:127], v[126:127], 1.0 op_sel_hi:[1,0]
	v_pk_add_f32 v[134:135], v[120:121], 1.0 op_sel_hi:[1,0]
	v_pk_add_f32 v[116:117], v[116:117], 1.0 op_sel_hi:[1,0]
	v_pk_add_f32 v[120:121], v[120:121], 1.0 op_sel_hi:[1,0] neg_lo:[1,0] neg_hi:[1,0]
	v_exp_f32_e32 v128, v128
	v_exp_f32_e32 v129, v129
	v_exp_f32_e32 v118, v118
	v_exp_f32_e32 v119, v119
	v_exp_f32_e32 v122, v122
	v_exp_f32_e32 v123, v123
	v_pk_mul_f32 v[126:127], v[126:127], v[134:135]
	v_exp_f32_e32 v130, v130
	v_exp_f32_e32 v131, v131
	v_pk_add_f32 v[128:129], v[128:129], 1.0 op_sel_hi:[1,0]
	v_pk_add_f32 v[136:137], v[122:123], 1.0 op_sel_hi:[1,0]
	v_pk_add_f32 v[118:119], v[118:119], 1.0 op_sel_hi:[1,0]
	v_pk_add_f32 v[122:123], v[122:123], 1.0 op_sel_hi:[1,0] neg_lo:[1,0] neg_hi:[1,0]
	v_rcp_f32_e32 v126, v126
	v_rcp_f32_e32 v127, v127
	v_rcp_f32_e32 v116, v116
	v_rcp_f32_e32 v117, v117
	v_pk_mul_f32 v[128:129], v[128:129], v[136:137]
	v_exp_f32_e32 v132, v132
	v_exp_f32_e32 v133, v133
	v_pk_mul_f32 v[120:121], v[120:121], v[126:127]
	v_pk_add_f32 v[130:131], v[130:131], 1.0 op_sel_hi:[1,0]
	v_rcp_f32_e32 v128, v128
	v_rcp_f32_e32 v129, v129
	v_rcp_f32_e32 v118, v118
	v_rcp_f32_e32 v119, v119
	v_pk_fma_f32 v[168:169], v[168:169], v[116:117], v[120:121]
	v_pk_mul_f32 v[122:123], v[122:123], v[128:129]
	v_pk_add_f32 v[132:133], v[132:133], 1.0 op_sel_hi:[1,0]
	v_pk_mul_f32 v[134:135], v[168:169], s[78:79]
	v_pk_fma_f32 v[170:171], v[170:171], v[118:119], v[122:123]
	v_med3_f32 v134, v134, s55, v232
	v_med3_f32 v135, v135, s55, v232
	v_pk_mul_f32 v[136:137], v[170:171], s[78:79]
	v_add_u32_e32 v122, 0x100, v166
	v_mov_b32_e32 v123, v114
	v_lshl_add_u64 v[122:123], v[122:123], 1, s[30:31]
	v_exp_f32_e32 v134, v134
	v_exp_f32_e32 v135, v135
	v_med3_f32 v136, v136, s55, v232
	v_med3_f32 v137, v137, s55, v232
	v_pk_add_f32 v[126:127], v[134:135], 1.0 op_sel_hi:[1,0]
	v_pk_add_f32 v[134:135], v[134:135], 1.0 op_sel_hi:[1,0] neg_lo:[1,0] neg_hi:[1,0]
	v_exp_f32_e32 v136, v136
	v_exp_f32_e32 v137, v137
	v_pk_mul_f32 v[130:131], v[130:131], v[126:127]
	v_pk_add_f32 v[128:129], v[136:137], 1.0 op_sel_hi:[1,0]
	v_pk_add_f32 v[136:137], v[136:137], 1.0 op_sel_hi:[1,0] neg_lo:[1,0] neg_hi:[1,0]
	v_rcp_f32_e32 v130, v130
	v_rcp_f32_e32 v131, v131
	v_pk_mul_f32 v[132:133], v[132:133], v[128:129]
	v_pk_mul_f32 v[134:135], v[134:135], v[130:131]
	v_rcp_f32_e32 v132, v132
	v_rcp_f32_e32 v133, v133
	v_cvt_pk_bf16_f32 v120, v134, v135
	v_pk_mul_f32 v[136:137], v[136:137], v[132:133]
	v_pk_mul_f32 v[134:135], v[162:163], v[134:135]
	v_cvt_pk_bf16_f32 v121, v136, v137
	v_cvt_pk_bf16_f32 v116, v134, v135
	v_pk_mul_f32 v[136:137], v[164:165], v[136:137]
	global_store_dwordx2 v[122:123], v[120:121], off nt
	v_cvt_pk_bf16_f32 v117, v136, v137
	ds_write_b64 v205, v[116:117] offset:4608
	s_and_b64 s[72:73], exec, s[6:7]
	s_cbranch_scc1 .Lpf_skip_3
	ds_read_b128 v[250:253], v199 offset:9216
	ds_read_b128 v[120:123], v198 offset:57600
	ds_read_b128 v[124:127], v199 offset:9344
	ds_read_b128 v[246:249], v199 offset:9280
	ds_read_b128 v[128:131], v199 offset:9408

	.amdhsa_kernel _Z10rnn_kernelPKfS0_S0_S0_S0_S0_PKtS2_PfPtS3_
		.amdhsa_group_segment_fixed_size 0
		.amdhsa_private_segment_fixed_size 0
		.amdhsa_kernarg_size 88
		.amdhsa_user_sgpr_count 2
		.amdhsa_user_sgpr_dispatch_ptr 0
		.amdhsa_user_sgpr_queue_ptr 0
		.amdhsa_user_sgpr_kernarg_segment_ptr 1
		.amdhsa_user_sgpr_dispatch_id 0
		.amdhsa_user_sgpr_kernarg_preload_length 0
		.amdhsa_user_sgpr_kernarg_preload_offset 0
		.amdhsa_user_sgpr_private_segment_size 0
		.amdhsa_uses_dynamic_stack 0
		.amdhsa_enable_private_segment 0
		.amdhsa_system_sgpr_workgroup_id_x 1
		.amdhsa_system_sgpr_workgroup_id_y 0
		.amdhsa_system_sgpr_workgroup_id_z 0
		.amdhsa_system_sgpr_workgroup_info 0
		.amdhsa_system_vgpr_workitem_id 0
		.amdhsa_next_free_vgpr 256
		.amdhsa_next_free_sgpr 80
		.amdhsa_accum_offset 256
		.amdhsa_reserve_vcc 1
		.amdhsa_float_round_mode_32 0
		.amdhsa_float_round_mode_16_64 0
		.amdhsa_float_denorm_mode_32 3
		.amdhsa_float_denorm_mode_16_64 3
		.amdhsa_dx10_clamp 1
		.amdhsa_ieee_mode 1
		.amdhsa_fp16_overflow 0
		.amdhsa_tg_split 0
		.amdhsa_exception_fp_ieee_invalid_op 0
		.amdhsa_exception_fp_denorm_src 0
		.amdhsa_exception_fp_ieee_div_zero 0
		.amdhsa_exception_fp_ieee_overflow 0
		.amdhsa_exception_fp_ieee_underflow 0
		.amdhsa_exception_fp_ieee_inexact 0
		.amdhsa_exception_int_div_zero 0
	.end_amdhsa_kernel

amdhsa.kernels:
  - .agpr_count:     0
    .args:
      - .actual_access:  read_only
        .address_space:  global
        .offset:         0
        .size:           8
        .value_kind:     global_buffer
      - .actual_access:  read_only
        .address_space:  global
        .offset:         8
        .size:           8
        .value_kind:     global_buffer
      - .actual_access:  read_only
        .address_space:  global
        .offset:         16
        .size:           8
        .value_kind:     global_buffer
      - .actual_access:  read_only
        .address_space:  global
        .offset:         24
        .size:           8
        .value_kind:     global_buffer
      - .actual_access:  read_only
        .address_space:  global
        .offset:         32
        .size:           8
        .value_kind:     global_buffer
      - .actual_access:  read_only
        .address_space:  global
        .offset:         40
        .size:           8
        .value_kind:     global_buffer
      - .actual_access:  read_only
        .address_space:  global
        .offset:         48
        .size:           8
        .value_kind:     global_buffer
      - .actual_access:  read_only
        .address_space:  global
        .offset:         56
        .size:           8
        .value_kind:     global_buffer
      - .actual_access:  read_only
        .address_space:  global
        .offset:         64
        .size:           8
        .value_kind:     global_buffer
      - .actual_access:  read_only
        .address_space:  global
        .offset:         72
        .size:           8
        .value_kind:     global_buffer
      - .actual_access:  read_only
        .address_space:  global
        .offset:         80
        .size:           8
        .value_kind:     global_buffer
      - .actual_access:  read_only
        .address_space:  global
        .offset:         88
        .size:           8
        .value_kind:     global_buffer
      - .actual_access:  read_only
        .address_space:  global
        .offset:         96
        .size:           8
        .value_kind:     global_buffer
      - .actual_access:  read_only
        .address_space:  global
        .offset:         104
        .size:           8
        .value_kind:     global_buffer
      - .actual_access:  read_only
        .address_space:  global
        .offset:         112
        .size:           8
        .value_kind:     global_buffer
      - .actual_access:  read_only
        .address_space:  global
        .offset:         120
        .size:           8
        .value_kind:     global_buffer
      - .actual_access:  write_only
        .address_space:  global
        .offset:         128
        .size:           8
        .value_kind:     global_buffer
      - .actual_access:  write_only
        .address_space:  global
        .offset:         136
        .size:           8
        .value_kind:     global_buffer
      - .actual_access:  write_only
        .address_space:  global
        .offset:         144
        .size:           8
        .value_kind:     global_buffer
    .group_segment_fixed_size: 0
    .kernarg_segment_align: 8
    .kernarg_segment_size: 152
    .language:       OpenCL C
    .language_version:
      - 2
      - 0
    .max_flat_workgroup_size: 256
    .name:           _Z11prep_kernelPKfS0_S0_S0_S0_S0_S0_S0_S0_S0_S0_S0_S0_S0_S0_S0_PtS1_S1_
    .private_segment_fixed_size: 0
    .sgpr_count:     30
    .sgpr_spill_count: 0
    .symbol:         _Z11prep_kernelPKfS0_S0_S0_S0_S0_S0_S0_S0_S0_S0_S0_S0_S0_S0_S0_PtS1_S1_.kd
    .uniform_work_group_size: 1
    .uses_dynamic_stack: false
    .vgpr_count:     8
    .vgpr_spill_count: 0
    .wavefront_size: 64
  - .agpr_count:     0
    .args:
      - .actual_access:  read_only
        .address_space:  global
        .offset:         0
        .size:           8
        .value_kind:     global_buffer
      - .actual_access:  read_only
        .address_space:  global
        .offset:         8
        .size:           8
        .value_kind:     global_buffer
      - .actual_access:  read_only
        .address_space:  global
        .offset:         16
        .size:           8
        .value_kind:     global_buffer
      - .actual_access:  read_only
        .address_space:  global
        .offset:         24
        .size:           8
        .value_kind:     global_buffer
      - .actual_access:  read_only
        .address_space:  global
        .offset:         32
        .size:           8
        .value_kind:     global_buffer
      - .actual_access:  read_only
        .address_space:  global
        .offset:         40
        .size:           8
        .value_kind:     global_buffer
      - .actual_access:  read_only
        .address_space:  global
        .offset:         48
        .size:           8
        .value_kind:     global_buffer
      - .actual_access:  read_only
        .address_space:  global
        .offset:         56
        .size:           8
        .value_kind:     global_buffer
      - .actual_access:  write_only
        .address_space:  global
        .offset:         64
        .size:           8
        .value_kind:     global_buffer
      - .actual_access:  write_only
        .address_space:  global
        .offset:         72
        .size:           8
        .value_kind:     global_buffer
      - .actual_access:  write_only
        .address_space:  global
        .offset:         80
        .size:           8
        .value_kind:     global_buffer
    .group_segment_fixed_size: 0
    .kernarg_segment_align: 8
    .kernarg_segment_size: 88
    .language:       OpenCL C
    .language_version:
      - 2
      - 0
    .max_flat_workgroup_size: 512
    .name:           _Z10rnn_kernelPKfS0_S0_S0_S0_S0_PKtS2_PfPtS3_
    .private_segment_fixed_size: 0
    .sgpr_count:     86
    .sgpr_spill_count: 0
    .symbol:         _Z10rnn_kernelPKfS0_S0_S0_S0_S0_PKtS2_PfPtS3_.kd
    .uniform_work_group_size: 1
    .uses_dynamic_stack: false
    .vgpr_count:     256
    .vgpr_spill_count: 0
    .wavefront_size: 64
  - .agpr_count:     0
    .args:
      - .actual_access:  read_only
        .address_space:  global
        .offset:         0
        .size:           8
        .value_kind:     global_buffer
      - .actual_access:  read_only
        .address_space:  global
        .offset:         8
        .size:           8
        .value_kind:     global_buffer
      - .actual_access:  read_only
        .address_space:  global
        .offset:         16
        .size:           8
        .value_kind:     global_buffer
      - .actual_access:  read_only
        .address_space:  global
        .offset:         24
        .size:           8
        .value_kind:     global_buffer
      - .actual_access:  read_only
        .address_space:  global
        .offset:         32
        .size:           8
        .value_kind:     global_buffer
      - .actual_access:  write_only
        .address_space:  global
        .offset:         40
        .size:           8
        .value_kind:     global_buffer
      - .actual_access:  write_only
        .address_space:  global
        .offset:         48
        .size:           8
        .value_kind:     global_buffer
    .group_segment_fixed_size: 0
    .kernarg_segment_align: 8
    .kernarg_segment_size: 56
    .language:       OpenCL C
    .language_version:
      - 2
      - 0
    .max_flat_workgroup_size: 1024
    .name:           _Z11attn_kernelPKtS0_PKfS2_S2_PfS3_
    .private_segment_fixed_size: 0
    .sgpr_count:     30
    .sgpr_spill_count: 0
    .symbol:         _Z11attn_kernelPKtS0_PKfS2_S2_PfS3_.kd
    .uniform_work_group_size: 1
    .uses_dynamic_stack: false
    .vgpr_count:     124
    .vgpr_spill_count: 0
    .wavefront_size: 64
  - .agpr_count:     0
    .args:
      - .actual_access:  read_only
        .address_space:  global
        .offset:         0
        .size:           8
        .value_kind:     global_buffer
      - .actual_access:  read_only
        .address_space:  global
        .offset:         8
        .size:           8
        .value_kind:     global_buffer
      - .actual_access:  read_only
        .address_space:  global
        .offset:         16
        .size:           8
        .value_kind:     global_buffer
      - .actual_access:  write_only
        .address_space:  global
        .offset:         24
        .size:           8
        .value_kind:     global_buffer
    .group_segment_fixed_size: 192
    .kernarg_segment_align: 8
    .kernarg_segment_size: 32
    .language:       OpenCL C
    .language_version:
      - 2
      - 0
    .max_flat_workgroup_size: 1024
    .name:           _Z11loss_kernelPKfS0_S0_Pf
    .private_segment_fixed_size: 0
    .sgpr_count:     14
    .sgpr_spill_count: 0
    .symbol:         _Z11loss_kernelPKfS0_S0_Pf.kd
    .uniform_work_group_size: 1
    .uses_dynamic_stack: false
    .vgpr_count:     46
    .vgpr_spill_count: 0
    .wavefront_size: 64
